# P2 score-table setup: the 27 table loads of a thread issued together and waited once instead of one exposed round trip per entry
# speedup vs baseline: 1.0162x; 1.0038x over previous
.LBB0_420:
	s_waitcnt vmcnt(0)
	s_mov_b64 s[10:11], exec
	s_movk_i32 s8, 0x404
	s_mov_b32 s6, 0xcc29786d
	v_mul_hi_u32 v125, v0, s6
	v_lshrrev_b32_e32 v125, 8, v125
	v_mul_u32_u24_e32 v126, 0x141, v125
	v_sub_u32_e32 v126, v0, v126
	v_subrev_u32_e32 v81, 32, v126
	v_lshlrev_b32_e32 v126, 2, v126
	v_mad_u32_u24 v127, v125, s8, v126
	s_movk_i32 s6, 0x101
	v_cmp_gt_u32_e32 vcc, s6, v81
	v_mov_b32_e32 v70, 0xff61b1e6
	s_and_saveexec_b64 s[6:7], vcc
	global_load_dword v70, v127, s[72:73] offset:-128
	s_mov_b64 exec, s[10:11]
	v_add_u32_e32 v124, 0x200, v0
	s_mov_b32 s6, 0xcc29786d
	v_mul_hi_u32 v125, v124, s6
	v_lshrrev_b32_e32 v125, 8, v125
	v_mul_u32_u24_e32 v126, 0x141, v125
	v_sub_u32_e32 v126, v124, v126
	v_subrev_u32_e32 v82, 32, v126
	v_lshlrev_b32_e32 v126, 2, v126
	v_mad_u32_u24 v127, v125, s8, v126
	s_movk_i32 s6, 0x101
	v_cmp_gt_u32_e32 vcc, s6, v82
	v_mov_b32_e32 v71, 0xff61b1e6
	s_and_saveexec_b64 s[6:7], vcc
	global_load_dword v71, v127, s[72:73] offset:-128
	s_mov_b64 exec, s[10:11]
	v_add_u32_e32 v124, 0x400, v0
	s_mov_b32 s6, 0xcc29786d
	v_mul_hi_u32 v125, v124, s6
	v_lshrrev_b32_e32 v125, 8, v125
	v_mul_u32_u24_e32 v126, 0x141, v125
	v_sub_u32_e32 v126, v124, v126
	v_subrev_u32_e32 v83, 32, v126
	v_lshlrev_b32_e32 v126, 2, v126
	v_mad_u32_u24 v127, v125, s8, v126
	s_movk_i32 s6, 0x101
	v_cmp_gt_u32_e32 vcc, s6, v83
	v_mov_b32_e32 v72, 0xff61b1e6
	s_and_saveexec_b64 s[6:7], vcc
	global_load_dword v72, v127, s[72:73] offset:-128
	s_mov_b64 exec, s[10:11]
	v_add_u32_e32 v124, 0x600, v0
	s_mov_b32 s6, 0xcc29786d
	v_mul_hi_u32 v125, v124, s6
	v_lshrrev_b32_e32 v125, 8, v125
	v_mul_u32_u24_e32 v126, 0x141, v125
	v_sub_u32_e32 v126, v124, v126
	v_subrev_u32_e32 v84, 32, v126
	v_lshlrev_b32_e32 v126, 2, v126
	v_mad_u32_u24 v127, v125, s8, v126
	s_movk_i32 s6, 0x101
	v_cmp_gt_u32_e32 vcc, s6, v84
	v_mov_b32_e32 v73, 0xff61b1e6
	s_and_saveexec_b64 s[6:7], vcc
	global_load_dword v73, v127, s[72:73] offset:-128
	s_mov_b64 exec, s[10:11]
	v_add_u32_e32 v124, 0x800, v0
	s_mov_b32 s6, 0xcc29786d
	v_mul_hi_u32 v125, v124, s6
	v_lshrrev_b32_e32 v125, 8, v125
	v_mul_u32_u24_e32 v126, 0x141, v125
	v_sub_u32_e32 v126, v124, v126
	v_subrev_u32_e32 v85, 32, v126
	v_lshlrev_b32_e32 v126, 2, v126
	v_mad_u32_u24 v127, v125, s8, v126
	s_movk_i32 s6, 0x101
	v_cmp_gt_u32_e32 vcc, s6, v85
	v_mov_b32_e32 v74, 0xff61b1e6
	s_and_saveexec_b64 s[6:7], vcc
	global_load_dword v74, v127, s[72:73] offset:-128
	s_mov_b64 exec, s[10:11]
	v_add_u32_e32 v124, 0xa00, v0
	s_mov_b32 s6, 0xcc29786d
	v_mul_hi_u32 v125, v124, s6
	v_lshrrev_b32_e32 v125, 8, v125
	v_mul_u32_u24_e32 v126, 0x141, v125
	v_sub_u32_e32 v126, v124, v126
	v_subrev_u32_e32 v86, 32, v126
	v_lshlrev_b32_e32 v126, 2, v126
	v_mad_u32_u24 v127, v125, s8, v126
	s_movk_i32 s6, 0x101
	v_cmp_gt_u32_e32 vcc, s6, v86
	v_mov_b32_e32 v75, 0xff61b1e6
	s_and_saveexec_b64 s[6:7], vcc
	global_load_dword v75, v127, s[72:73] offset:-128
	s_mov_b64 exec, s[10:11]
	v_add_u32_e32 v124, 0xc00, v0
	s_mov_b32 s6, 0xcc29786d
	v_mul_hi_u32 v125, v124, s6
	v_lshrrev_b32_e32 v125, 8, v125
	v_mul_u32_u24_e32 v126, 0x141, v125
	v_sub_u32_e32 v126, v124, v126
	v_subrev_u32_e32 v87, 32, v126
	v_lshlrev_b32_e32 v126, 2, v126
	v_mad_u32_u24 v127, v125, s8, v126
	s_movk_i32 s6, 0x101
	v_cmp_gt_u32_e32 vcc, s6, v87
	v_mov_b32_e32 v76, 0xff61b1e6
	s_and_saveexec_b64 s[6:7], vcc
	global_load_dword v76, v127, s[72:73] offset:-128
	s_mov_b64 exec, s[10:11]
	v_add_u32_e32 v124, 0xe00, v0
	s_mov_b32 s6, 0xcc29786d
	v_mul_hi_u32 v125, v124, s6
	v_lshrrev_b32_e32 v125, 8, v125
	v_mul_u32_u24_e32 v126, 0x141, v125
	v_sub_u32_e32 v126, v124, v126
	v_subrev_u32_e32 v88, 32, v126
	v_lshlrev_b32_e32 v126, 2, v126
	v_mad_u32_u24 v127, v125, s8, v126
	s_movk_i32 s6, 0x101
	v_cmp_gt_u32_e32 vcc, s6, v88
	v_mov_b32_e32 v77, 0xff61b1e6
	s_and_saveexec_b64 s[6:7], vcc
	global_load_dword v77, v127, s[72:73] offset:-128
	s_mov_b64 exec, s[10:11]
	v_add_u32_e32 v124, 0x1000, v0
	s_mov_b32 s6, 0xcc29786d
	v_mul_hi_u32 v125, v124, s6
	v_lshrrev_b32_e32 v125, 8, v125
	v_mul_u32_u24_e32 v126, 0x141, v125
	v_sub_u32_e32 v126, v124, v126
	v_subrev_u32_e32 v89, 32, v126
	v_lshlrev_b32_e32 v126, 2, v126
	v_mad_u32_u24 v127, v125, s8, v126
	s_movk_i32 s6, 0x101
	v_cmp_gt_u32_e32 vcc, s6, v89
	v_mov_b32_e32 v78, 0xff61b1e6
	s_and_saveexec_b64 s[6:7], vcc
	global_load_dword v78, v127, s[72:73] offset:-128
	s_mov_b64 exec, s[10:11]
	v_add_u32_e32 v124, 0x1200, v0
	s_mov_b32 s6, 0xcc29786d
	v_mul_hi_u32 v125, v124, s6
	v_lshrrev_b32_e32 v125, 8, v125
	v_mul_u32_u24_e32 v126, 0x141, v125
	v_sub_u32_e32 v126, v124, v126
	v_subrev_u32_e32 v90, 32, v126
	v_lshlrev_b32_e32 v126, 2, v126
	v_mad_u32_u24 v127, v125, s8, v126
	s_movk_i32 s6, 0x101
	v_cmp_gt_u32_e32 vcc, s6, v90
	v_mov_b32_e32 v79, 0xff61b1e6
	s_and_saveexec_b64 s[6:7], vcc
	global_load_dword v79, v127, s[72:73] offset:-128
	s_mov_b64 exec, s[10:11]
	v_add_u32_e32 v124, 0x1400, v0
	s_mov_b32 s6, 0xcc29786d
	v_mul_hi_u32 v125, v124, s6
	v_lshrrev_b32_e32 v125, 8, v125
	v_mul_u32_u24_e32 v126, 0x141, v125
	v_sub_u32_e32 v126, v124, v126
	v_subrev_u32_e32 v91, 32, v126
	v_lshlrev_b32_e32 v126, 2, v126
	v_mad_u32_u24 v127, v125, s8, v126
	s_movk_i32 s6, 0x101
	v_cmp_gt_u32_e32 vcc, s6, v91
	v_mov_b32_e32 v80, 0xff61b1e6
	s_and_saveexec_b64 s[6:7], vcc
	global_load_dword v80, v127, s[72:73] offset:-128
	s_mov_b64 exec, s[10:11]
	s_mov_b32 s6, 0x663d81
	v_mul_hi_u32 v125, v0, s6
	v_mul_u32_u24_e32 v126, 0x281, v125
	v_sub_u32_e32 v126, v0, v126
	v_add_u32_e32 v108, 0xffffff00, v126
	v_lshlrev_b32_e32 v126, 2, v126
	v_lshrrev_b32_e32 v128, 2, v125
	v_and_b32_e32 v125, 3, v125
	s_movk_i32 s6, 0x810
	v_mad_u32_u24 v127, v128, s6, v126
	s_movk_i32 s6, 0x204
	v_mad_u32_u24 v127, v125, s6, v127
	v_add_u32_e32 v127, 0x103000, v127
	s_movk_i32 s6, 0x81
	v_cmp_gt_u32_e32 vcc, s6, v108
	v_mov_b32_e32 v92, 0xff61b1e6
	s_and_saveexec_b64 s[6:7], vcc
	global_load_dword v92, v127, s[90:91] offset:3136
	s_mov_b64 exec, s[10:11]
	v_add_u32_e32 v124, 0x200, v0
	s_mov_b32 s6, 0x663d81
	v_mul_hi_u32 v125, v124, s6
	v_mul_u32_u24_e32 v126, 0x281, v125
	v_sub_u32_e32 v126, v124, v126
	v_add_u32_e32 v109, 0xffffff00, v126
	v_lshlrev_b32_e32 v126, 2, v126
	v_lshrrev_b32_e32 v128, 2, v125
	v_and_b32_e32 v125, 3, v125
	s_movk_i32 s6, 0x810
	v_mad_u32_u24 v127, v128, s6, v126
	s_movk_i32 s6, 0x204
	v_mad_u32_u24 v127, v125, s6, v127
	v_add_u32_e32 v127, 0x103000, v127
	s_movk_i32 s6, 0x81
	v_cmp_gt_u32_e32 vcc, s6, v109
	v_mov_b32_e32 v93, 0xff61b1e6
	s_and_saveexec_b64 s[6:7], vcc
	global_load_dword v93, v127, s[90:91] offset:3136
	s_mov_b64 exec, s[10:11]
	v_add_u32_e32 v124, 0x400, v0
	s_mov_b32 s6, 0x663d81
	v_mul_hi_u32 v125, v124, s6
	v_mul_u32_u24_e32 v126, 0x281, v125
	v_sub_u32_e32 v126, v124, v126
	v_add_u32_e32 v110, 0xffffff00, v126
	v_lshlrev_b32_e32 v126, 2, v126
	v_lshrrev_b32_e32 v128, 2, v125
	v_and_b32_e32 v125, 3, v125
	s_movk_i32 s6, 0x810
	v_mad_u32_u24 v127, v128, s6, v126
	s_movk_i32 s6, 0x204
	v_mad_u32_u24 v127, v125, s6, v127
	v_add_u32_e32 v127, 0x103000, v127
	s_movk_i32 s6, 0x81
	v_cmp_gt_u32_e32 vcc, s6, v110
	v_mov_b32_e32 v94, 0xff61b1e6
	s_and_saveexec_b64 s[6:7], vcc
	global_load_dword v94, v127, s[90:91] offset:3136
	s_mov_b64 exec, s[10:11]
	v_add_u32_e32 v124, 0x600, v0
	s_mov_b32 s6, 0x663d81
	v_mul_hi_u32 v125, v124, s6
	v_mul_u32_u24_e32 v126, 0x281, v125
	v_sub_u32_e32 v126, v124, v126
	v_add_u32_e32 v111, 0xffffff00, v126
	v_lshlrev_b32_e32 v126, 2, v126
	v_lshrrev_b32_e32 v128, 2, v125
	v_and_b32_e32 v125, 3, v125
	s_movk_i32 s6, 0x810
	v_mad_u32_u24 v127, v128, s6, v126
	s_movk_i32 s6, 0x204
	v_mad_u32_u24 v127, v125, s6, v127
	v_add_u32_e32 v127, 0x103000, v127
	s_movk_i32 s6, 0x81
	v_cmp_gt_u32_e32 vcc, s6, v111
	v_mov_b32_e32 v95, 0xff61b1e6
	s_and_saveexec_b64 s[6:7], vcc
	global_load_dword v95, v127, s[90:91] offset:3136
	s_mov_b64 exec, s[10:11]
	v_add_u32_e32 v124, 0x800, v0
	s_mov_b32 s6, 0x663d81
	v_mul_hi_u32 v125, v124, s6
	v_mul_u32_u24_e32 v126, 0x281, v125
	v_sub_u32_e32 v126, v124, v126
	v_add_u32_e32 v112, 0xffffff00, v126
	v_lshlrev_b32_e32 v126, 2, v126
	v_lshrrev_b32_e32 v128, 2, v125
	v_and_b32_e32 v125, 3, v125
	s_movk_i32 s6, 0x810
	v_mad_u32_u24 v127, v128, s6, v126
	s_movk_i32 s6, 0x204
	v_mad_u32_u24 v127, v125, s6, v127
	v_add_u32_e32 v127, 0x103000, v127
	s_movk_i32 s6, 0x81
	v_cmp_gt_u32_e32 vcc, s6, v112
	v_mov_b32_e32 v96, 0xff61b1e6
	s_and_saveexec_b64 s[6:7], vcc
	global_load_dword v96, v127, s[90:91] offset:3136
	s_mov_b64 exec, s[10:11]
	v_add_u32_e32 v124, 0xa00, v0
	s_mov_b32 s6, 0x663d81
	v_mul_hi_u32 v125, v124, s6
	v_mul_u32_u24_e32 v126, 0x281, v125
	v_sub_u32_e32 v126, v124, v126
	v_add_u32_e32 v113, 0xffffff00, v126
	v_lshlrev_b32_e32 v126, 2, v126
	v_lshrrev_b32_e32 v128, 2, v125
	v_and_b32_e32 v125, 3, v125
	s_movk_i32 s6, 0x810
	v_mad_u32_u24 v127, v128, s6, v126
	s_movk_i32 s6, 0x204
	v_mad_u32_u24 v127, v125, s6, v127
	v_add_u32_e32 v127, 0x103000, v127
	s_movk_i32 s6, 0x81
	v_cmp_gt_u32_e32 vcc, s6, v113
	v_mov_b32_e32 v97, 0xff61b1e6
	s_and_saveexec_b64 s[6:7], vcc
	global_load_dword v97, v127, s[90:91] offset:3136
	s_mov_b64 exec, s[10:11]
	v_add_u32_e32 v124, 0xc00, v0
	s_mov_b32 s6, 0x663d81
	v_mul_hi_u32 v125, v124, s6
	v_mul_u32_u24_e32 v126, 0x281, v125
	v_sub_u32_e32 v126, v124, v126
	v_add_u32_e32 v114, 0xffffff00, v126
	v_lshlrev_b32_e32 v126, 2, v126
	v_lshrrev_b32_e32 v128, 2, v125
	v_and_b32_e32 v125, 3, v125
	s_movk_i32 s6, 0x810
	v_mad_u32_u24 v127, v128, s6, v126
	s_movk_i32 s6, 0x204
	v_mad_u32_u24 v127, v125, s6, v127
	v_add_u32_e32 v127, 0x103000, v127
	s_movk_i32 s6, 0x81
	v_cmp_gt_u32_e32 vcc, s6, v114
	v_mov_b32_e32 v98, 0xff61b1e6
	s_and_saveexec_b64 s[6:7], vcc
	global_load_dword v98, v127, s[90:91] offset:3136
	s_mov_b64 exec, s[10:11]
	v_add_u32_e32 v124, 0xe00, v0
	s_mov_b32 s6, 0x663d81
	v_mul_hi_u32 v125, v124, s6
	v_mul_u32_u24_e32 v126, 0x281, v125
	v_sub_u32_e32 v126, v124, v126
	v_add_u32_e32 v115, 0xffffff00, v126
	v_lshlrev_b32_e32 v126, 2, v126
	v_lshrrev_b32_e32 v128, 2, v125
	v_and_b32_e32 v125, 3, v125
	s_movk_i32 s6, 0x810
	v_mad_u32_u24 v127, v128, s6, v126
	s_movk_i32 s6, 0x204
	v_mad_u32_u24 v127, v125, s6, v127
	v_add_u32_e32 v127, 0x103000, v127
	s_movk_i32 s6, 0x81
	v_cmp_gt_u32_e32 vcc, s6, v115
	v_mov_b32_e32 v99, 0xff61b1e6
	s_and_saveexec_b64 s[6:7], vcc
	global_load_dword v99, v127, s[90:91] offset:3136
	s_mov_b64 exec, s[10:11]
	v_add_u32_e32 v124, 0x1000, v0
	s_mov_b32 s6, 0x663d81
	v_mul_hi_u32 v125, v124, s6
	v_mul_u32_u24_e32 v126, 0x281, v125
	v_sub_u32_e32 v126, v124, v126
	v_add_u32_e32 v116, 0xffffff00, v126
	v_lshlrev_b32_e32 v126, 2, v126
	v_lshrrev_b32_e32 v128, 2, v125
	v_and_b32_e32 v125, 3, v125
	s_movk_i32 s6, 0x810
	v_mad_u32_u24 v127, v128, s6, v126
	s_movk_i32 s6, 0x204
	v_mad_u32_u24 v127, v125, s6, v127
	v_add_u32_e32 v127, 0x103000, v127
	s_movk_i32 s6, 0x81
	v_cmp_gt_u32_e32 vcc, s6, v116
	v_mov_b32_e32 v100, 0xff61b1e6
	s_and_saveexec_b64 s[6:7], vcc
	global_load_dword v100, v127, s[90:91] offset:3136
	s_mov_b64 exec, s[10:11]
	v_add_u32_e32 v124, 0x1200, v0
	s_mov_b32 s6, 0x663d81
	v_mul_hi_u32 v125, v124, s6
	v_mul_u32_u24_e32 v126, 0x281, v125
	v_sub_u32_e32 v126, v124, v126
	v_add_u32_e32 v117, 0xffffff00, v126
	v_lshlrev_b32_e32 v126, 2, v126
	v_lshrrev_b32_e32 v128, 2, v125
	v_and_b32_e32 v125, 3, v125
	s_movk_i32 s6, 0x810
	v_mad_u32_u24 v127, v128, s6, v126
	s_movk_i32 s6, 0x204
	v_mad_u32_u24 v127, v125, s6, v127
	v_add_u32_e32 v127, 0x103000, v127
	s_movk_i32 s6, 0x81
	v_cmp_gt_u32_e32 vcc, s6, v117
	v_mov_b32_e32 v101, 0xff61b1e6
	s_and_saveexec_b64 s[6:7], vcc
	global_load_dword v101, v127, s[90:91] offset:3136
	s_mov_b64 exec, s[10:11]
	v_add_u32_e32 v124, 0x1400, v0
	s_mov_b32 s6, 0x663d81
	v_mul_hi_u32 v125, v124, s6
	v_mul_u32_u24_e32 v126, 0x281, v125
	v_sub_u32_e32 v126, v124, v126
	v_add_u32_e32 v118, 0xffffff00, v126
	v_lshlrev_b32_e32 v126, 2, v126
	v_lshrrev_b32_e32 v128, 2, v125
	v_and_b32_e32 v125, 3, v125
	s_movk_i32 s6, 0x810
	v_mad_u32_u24 v127, v128, s6, v126
	s_movk_i32 s6, 0x204
	v_mad_u32_u24 v127, v125, s6, v127
	v_add_u32_e32 v127, 0x103000, v127
	s_movk_i32 s6, 0x81
	v_cmp_gt_u32_e32 vcc, s6, v118
	v_mov_b32_e32 v102, 0xff61b1e6
	s_and_saveexec_b64 s[6:7], vcc
	global_load_dword v102, v127, s[90:91] offset:3136
	s_mov_b64 exec, s[10:11]
	v_add_u32_e32 v124, 0x1600, v0
	s_mov_b32 s6, 0x663d81
	v_mul_hi_u32 v125, v124, s6
	v_mul_u32_u24_e32 v126, 0x281, v125
	v_sub_u32_e32 v126, v124, v126
	v_add_u32_e32 v119, 0xffffff00, v126
	v_lshlrev_b32_e32 v126, 2, v126
	v_lshrrev_b32_e32 v128, 2, v125
	v_and_b32_e32 v125, 3, v125
	s_movk_i32 s6, 0x810
	v_mad_u32_u24 v127, v128, s6, v126
	s_movk_i32 s6, 0x204
	v_mad_u32_u24 v127, v125, s6, v127
	v_add_u32_e32 v127, 0x103000, v127
	s_movk_i32 s6, 0x81
	v_cmp_gt_u32_e32 vcc, s6, v119
	v_mov_b32_e32 v103, 0xff61b1e6
	s_and_saveexec_b64 s[6:7], vcc
	global_load_dword v103, v127, s[90:91] offset:3136
	s_mov_b64 exec, s[10:11]
	v_add_u32_e32 v124, 0x1800, v0
	s_mov_b32 s6, 0x663d81
	v_mul_hi_u32 v125, v124, s6
	v_mul_u32_u24_e32 v126, 0x281, v125
	v_sub_u32_e32 v126, v124, v126
	v_add_u32_e32 v120, 0xffffff00, v126
	v_lshlrev_b32_e32 v126, 2, v126
	v_lshrrev_b32_e32 v128, 2, v125
	v_and_b32_e32 v125, 3, v125
	s_movk_i32 s6, 0x810
	v_mad_u32_u24 v127, v128, s6, v126
	s_movk_i32 s6, 0x204
	v_mad_u32_u24 v127, v125, s6, v127
	v_add_u32_e32 v127, 0x103000, v127
	s_movk_i32 s6, 0x81
	v_cmp_gt_u32_e32 vcc, s6, v120
	v_mov_b32_e32 v104, 0xff61b1e6
	s_and_saveexec_b64 s[6:7], vcc
	global_load_dword v104, v127, s[90:91] offset:3136
	s_mov_b64 exec, s[10:11]
	v_add_u32_e32 v124, 0x1a00, v0
	s_mov_b32 s6, 0x663d81
	v_mul_hi_u32 v125, v124, s6
	v_mul_u32_u24_e32 v126, 0x281, v125
	v_sub_u32_e32 v126, v124, v126
	v_add_u32_e32 v121, 0xffffff00, v126
	v_lshlrev_b32_e32 v126, 2, v126
	v_lshrrev_b32_e32 v128, 2, v125
	v_and_b32_e32 v125, 3, v125
	s_movk_i32 s6, 0x810
	v_mad_u32_u24 v127, v128, s6, v126
	s_movk_i32 s6, 0x204
	v_mad_u32_u24 v127, v125, s6, v127
	v_add_u32_e32 v127, 0x103000, v127
	s_movk_i32 s6, 0x81
	v_cmp_gt_u32_e32 vcc, s6, v121
	v_mov_b32_e32 v105, 0xff61b1e6
	s_and_saveexec_b64 s[6:7], vcc
	global_load_dword v105, v127, s[90:91] offset:3136
	s_mov_b64 exec, s[10:11]
	v_add_u32_e32 v124, 0x1c00, v0
	s_mov_b32 s6, 0x663d81
	v_mul_hi_u32 v125, v124, s6
	v_mul_u32_u24_e32 v126, 0x281, v125
	v_sub_u32_e32 v126, v124, v126
	v_add_u32_e32 v122, 0xffffff00, v126
	v_lshlrev_b32_e32 v126, 2, v126
	v_lshrrev_b32_e32 v128, 2, v125
	v_and_b32_e32 v125, 3, v125
	s_movk_i32 s6, 0x810
	v_mad_u32_u24 v127, v128, s6, v126
	s_movk_i32 s6, 0x204
	v_mad_u32_u24 v127, v125, s6, v127
	v_add_u32_e32 v127, 0x103000, v127
	s_movk_i32 s6, 0x81
	v_cmp_gt_u32_e32 vcc, s6, v122
	v_mov_b32_e32 v106, 0xff61b1e6
	s_and_saveexec_b64 s[6:7], vcc
	global_load_dword v106, v127, s[90:91] offset:3136
	s_mov_b64 exec, s[10:11]
	v_add_u32_e32 v124, 0x1e00, v0
	s_mov_b32 s6, 0x663d81
	v_mul_hi_u32 v125, v124, s6
	v_mul_u32_u24_e32 v126, 0x281, v125
	v_sub_u32_e32 v126, v124, v126
	v_add_u32_e32 v123, 0xffffff00, v126
	v_lshlrev_b32_e32 v126, 2, v126
	v_lshrrev_b32_e32 v128, 2, v125
	v_and_b32_e32 v125, 3, v125
	s_movk_i32 s6, 0x810
	v_mad_u32_u24 v127, v128, s6, v126
	s_movk_i32 s6, 0x204
	v_mad_u32_u24 v127, v125, s6, v127
	v_add_u32_e32 v127, 0x103000, v127
	s_movk_i32 s6, 0x81
	v_cmp_gt_u32_e32 vcc, s6, v123
	v_mov_b32_e32 v107, 0xff61b1e6
	s_and_saveexec_b64 s[6:7], vcc
	global_load_dword v107, v127, s[90:91] offset:3136
	s_mov_b64 exec, s[10:11]
	s_waitcnt vmcnt(0)
	s_movk_i32 s6, 0x101
	v_cmp_gt_u32_e32 vcc, s6, v81
	v_mul_f32_e32 v124, 0x3fb8aa3b, v70
	s_nop 0
	v_cndmask_b32_e32 v70, v70, v124, vcc
	ds_write_b32 v161, v70
	v_cmp_gt_u32_e32 vcc, s6, v82
	v_mul_f32_e32 v124, 0x3fb8aa3b, v71
	s_nop 0
	v_cndmask_b32_e32 v71, v71, v124, vcc
	ds_write_b32 v161, v71 offset:2048
	v_cmp_gt_u32_e32 vcc, s6, v83
	v_mul_f32_e32 v124, 0x3fb8aa3b, v72
	s_nop 0
	v_cndmask_b32_e32 v72, v72, v124, vcc
	ds_write_b32 v161, v72 offset:4096
	v_cmp_gt_u32_e32 vcc, s6, v84
	v_mul_f32_e32 v124, 0x3fb8aa3b, v73
	s_nop 0
	v_cndmask_b32_e32 v73, v73, v124, vcc
	ds_write_b32 v161, v73 offset:6144
	v_cmp_gt_u32_e32 vcc, s6, v85
	v_mul_f32_e32 v124, 0x3fb8aa3b, v74
	s_nop 0
	v_cndmask_b32_e32 v74, v74, v124, vcc
	ds_write_b32 v161, v74 offset:8192
	v_cmp_gt_u32_e32 vcc, s6, v86
	v_mul_f32_e32 v124, 0x3fb8aa3b, v75
	s_nop 0
	v_cndmask_b32_e32 v75, v75, v124, vcc
	ds_write_b32 v161, v75 offset:10240
	v_cmp_gt_u32_e32 vcc, s6, v87
	v_mul_f32_e32 v124, 0x3fb8aa3b, v76
	s_nop 0
	v_cndmask_b32_e32 v76, v76, v124, vcc
	ds_write_b32 v161, v76 offset:12288
	v_cmp_gt_u32_e32 vcc, s6, v88
	v_mul_f32_e32 v124, 0x3fb8aa3b, v77
	s_nop 0
	v_cndmask_b32_e32 v77, v77, v124, vcc
	ds_write_b32 v161, v77 offset:14336
	v_cmp_gt_u32_e32 vcc, s6, v89
	v_mul_f32_e32 v124, 0x3fb8aa3b, v78
	s_nop 0
	v_cndmask_b32_e32 v78, v78, v124, vcc
	ds_write_b32 v161, v78 offset:16384
	v_cmp_gt_u32_e32 vcc, s6, v90
	v_mul_f32_e32 v124, 0x3fb8aa3b, v79
	s_nop 0
	v_cndmask_b32_e32 v79, v79, v124, vcc
	ds_write_b32 v161, v79 offset:18432
	v_cmp_gt_u32_e32 vcc, s6, v91
	v_mul_f32_e32 v124, 0x3fb8aa3b, v80
	s_nop 0
	v_cndmask_b32_e32 v80, v80, v124, vcc
	v_cmp_gt_u32_e32 vcc, 16, v0
	s_and_saveexec_b64 s[0:1], vcc
	ds_write_b32 v161, v80 offset:20480
	s_mov_b64 exec, s[10:11]
	s_movk_i32 s6, 0x81
	v_cmp_gt_u32_e32 vcc, s6, v108
	v_mul_f32_e32 v124, 0x3fb8aa3b, v92
	s_nop 0
	v_cndmask_b32_e32 v92, v92, v124, vcc
	ds_write_b32 v180, v92
	v_cmp_gt_u32_e32 vcc, s6, v109
	v_mul_f32_e32 v124, 0x3fb8aa3b, v93
	s_nop 0
	v_cndmask_b32_e32 v93, v93, v124, vcc
	ds_write_b32 v180, v93 offset:2048
	v_cmp_gt_u32_e32 vcc, s6, v110
	v_mul_f32_e32 v124, 0x3fb8aa3b, v94
	s_nop 0
	v_cndmask_b32_e32 v94, v94, v124, vcc
	ds_write_b32 v180, v94 offset:4096
	v_cmp_gt_u32_e32 vcc, s6, v111
	v_mul_f32_e32 v124, 0x3fb8aa3b, v95
	s_nop 0
	v_cndmask_b32_e32 v95, v95, v124, vcc
	ds_write_b32 v180, v95 offset:6144
	v_cmp_gt_u32_e32 vcc, s6, v112
	v_mul_f32_e32 v124, 0x3fb8aa3b, v96
	s_nop 0
	v_cndmask_b32_e32 v96, v96, v124, vcc
	ds_write_b32 v180, v96 offset:8192
	v_cmp_gt_u32_e32 vcc, s6, v113
	v_mul_f32_e32 v124, 0x3fb8aa3b, v97
	s_nop 0
	v_cndmask_b32_e32 v97, v97, v124, vcc
	ds_write_b32 v180, v97 offset:10240
	v_cmp_gt_u32_e32 vcc, s6, v114
	v_mul_f32_e32 v124, 0x3fb8aa3b, v98
	s_nop 0
	v_cndmask_b32_e32 v98, v98, v124, vcc
	ds_write_b32 v180, v98 offset:12288
	v_cmp_gt_u32_e32 vcc, s6, v115
	v_mul_f32_e32 v124, 0x3fb8aa3b, v99
	s_nop 0
	v_cndmask_b32_e32 v99, v99, v124, vcc
	ds_write_b32 v180, v99 offset:14336
	v_cmp_gt_u32_e32 vcc, s6, v116
	v_mul_f32_e32 v124, 0x3fb8aa3b, v100
	s_nop 0
	v_cndmask_b32_e32 v100, v100, v124, vcc
	ds_write_b32 v180, v100 offset:16384
	v_cmp_gt_u32_e32 vcc, s6, v117
	v_mul_f32_e32 v124, 0x3fb8aa3b, v101
	s_nop 0
	v_cndmask_b32_e32 v101, v101, v124, vcc
	ds_write_b32 v180, v101 offset:18432
	v_cmp_gt_u32_e32 vcc, s6, v118
	v_mul_f32_e32 v124, 0x3fb8aa3b, v102
	s_nop 0
	v_cndmask_b32_e32 v102, v102, v124, vcc
	ds_write_b32 v180, v102 offset:20480
	v_cmp_gt_u32_e32 vcc, s6, v119
	v_mul_f32_e32 v124, 0x3fb8aa3b, v103
	s_nop 0
	v_cndmask_b32_e32 v103, v103, v124, vcc
	ds_write_b32 v180, v103 offset:22528
	v_cmp_gt_u32_e32 vcc, s6, v120
	v_mul_f32_e32 v124, 0x3fb8aa3b, v104
	s_nop 0
	v_cndmask_b32_e32 v104, v104, v124, vcc
	ds_write_b32 v180, v104 offset:24576
	v_cmp_gt_u32_e32 vcc, s6, v121
	v_mul_f32_e32 v124, 0x3fb8aa3b, v105
	s_nop 0
	v_cndmask_b32_e32 v105, v105, v124, vcc
	ds_write_b32 v180, v105 offset:26624
	v_cmp_gt_u32_e32 vcc, s6, v122
	v_mul_f32_e32 v124, 0x3fb8aa3b, v106
	s_nop 0
	v_cndmask_b32_e32 v106, v106, v124, vcc
	ds_write_b32 v180, v106 offset:28672
	v_cmp_gt_u32_e32 vcc, s6, v123
	v_mul_f32_e32 v124, 0x3fb8aa3b, v107
	s_nop 0
	v_cndmask_b32_e32 v107, v107, v124, vcc
	v_cmp_gt_u32_e32 vcc, 12, v0
	s_and_saveexec_b64 s[0:1], vcc
	ds_write_b32 v180, v107 offset:30720
	s_mov_b64 exec, s[10:11]
	s_mov_b64 s[0:1], exec
